# S5 scan loop restructured (LDS operand reads hoisted, u sub-tiles via LDS-DMA ring) + S5 parameter arrays prefetched at phase start
# speedup vs baseline: 1.0136x; 1.0033x over previous
; __global__ void __launch_bounds__(NWAVES * 64, 2) mk_fwd(Args args) {
;     ...
;             for (int item = bid; item < 256; item += G) {
;                 const int b = item >> 6, g = item & 63;
;                 const float dt = expf(ka->in[12][l * 64 + g]);
;                 float ab_re, ab_im;
;                 { const float lam_re = fminf(ka->in[6][(l * 64 + g) * 64 + lane], -1e-4f), lam_im = ka->in[7][(l * 64 + g) * 64 + lane];
;                   const float mag = expf(lam_re * dt); ab_re = mag * cosf(lam_im * dt); ab_im = mag * sinf(lam_im * dt); }
;                 pg8::bf16x8 Abb[8];
; #pragma unroll
;                 for (int mt = 0; mt < 4; ++mt) {
;                     const int pp = 16 * mt + i16;
;                     const float lam_re = fminf(ka->in[6][(l * 64 + g) * 64 + pp], -1e-4f), lam_im = ka->in[7][(l * 64 + g) * 64 + pp];
;                     const float mag = expf(lam_re * dt), are = mag * cosf(lam_im * dt), aim = mag * sinf(lam_im * dt);
;                     const float den = lam_re * lam_re + lam_im * lam_im, nre = are - 1.0f;
;                     const float cr = (nre * lam_re + aim * lam_im) / den, ci = (aim * lam_re - nre * lam_im) / den;
;                     v4u wr_ = {0u, 0u, 0u, 0u}, wi_ = {0u, 0u, 0u, 0u};
;                     if (g4 < 2) {
;                         const float* bre = ka->in[8] + ((size_t)(l * 64 + g) * 64 + pp) * 16 + 8 * g4; const float* bim = ka->in[9] + ((size_t)(l * 64 + g) * 64 + pp) * 16 + 8 * g4;
;                         const f32x4 r0 = *(const f32x4*)bre, r1 = *(const f32x4*)(bre + 4), m0_ = *(const f32x4*)bim, m1_ = *(const f32x4*)(bim + 4);
;                         const f32x4 xr0 = cr * r0 - ci * m0_, xr1 = cr * r1 - ci * m1_, xi0 = cr * m0_ + ci * r0, xi1 = cr * m1_ + ci * r1;
;                         wr_.x = cvt_pk_bf16(xr0[0], xr0[1]); wr_.y = cvt_pk_bf16(xr0[2], xr0[3]); wr_.z = cvt_pk_bf16(xr1[0], xr1[1]); wr_.w = cvt_pk_bf16(xr1[2], xr1[3]);
;                         wi_.x = cvt_pk_bf16(xi0[0], xi0[1]); wi_.y = cvt_pk_bf16(xi0[2], xi0[3]); wi_.z = cvt_pk_bf16(xi1[0], xi1[1]); wi_.w = cvt_pk_bf16(xi1[2], xi1[3]);
;                     }
;                     Abb[mt] = __builtin_bit_cast(pg8::bf16x8, wr_); Abb[4 + mt] = __builtin_bit_cast(pg8::bf16x8, wi_);
;                 }
;                 pg8::bf16x8 Cop[4];
; #pragma unroll
;                 for (int kb = 0; kb < 4; ++kb) {
.LBB0_410:
	s_mov_b32 s2, s80
	s_cmp_gt_i32 s76, s2
	s_cselect_b64 s[0:1], -1, 0
	s_cmp_ge_i32 s2, s77
	s_cselect_b64 s[2:3], -1, 0
	s_or_b64 s[0:1], s[0:1], s[2:3]
	s_and_b64 vcc, exec, s[0:1]
	s_cbranch_vccnz .LBB0_505
	v_readlane_b32 s0, v254, 8
	v_readlane_b32 s2, v254, 10
	v_readlane_b32 s1, v254, 9
	v_mbcnt_lo_u32_b32 v65, -1, 0
	v_mbcnt_hi_u32_b32 v65, -1, v65
	s_load_dword s3, s[0:1], 0x0
	s_mov_b32 s34, s84
	v_readlane_b32 s0, v254, 0
	s_waitcnt lgkmcnt(0)
	v_readlane_b32 s1, v254, 1
	s_cmpk_gt_i32 s34, 0xff
	s_cbranch_scc1 .LBB0_505
	s_load_dwordx8 s[4:11], s[0:1], 0x30
	s_load_dwordx4 s[12:15], s[0:1], 0x50
	v_readlane_b32 s16, v254, 38
	s_nop 3
	s_lshl_b32 s16, s16, 6
	s_and_b32 s17, s34, 63
	s_add_i32 s16, s16, s17
	s_lshl_b32 s17, s16, 8
	s_lshl_b32 s16, s16, 12
	v_lshl_add_u32 v240, v65, 2, s17
	v_lshl_add_u32 v241, v65, 6, s16
	s_waitcnt lgkmcnt(0)
	global_load_dword v242, v240, s[4:5]
	global_load_dword v243, v240, s[6:7]
	global_load_dword v244, v241, s[8:9]
	global_load_dword v245, v241, s[10:11]
	global_load_dword v246, v241, s[12:13]
	global_load_dword v247, v241, s[14:15]
	s_load_dwordx2 s[8:9], s[0:1], 0x138
	v_ashrrev_i32_e32 v3, 4, v65
	v_lshlrev_b32_e32 v66, 2, v3
	v_ashrrev_i32_e32 v67, 31, v66
	s_mul_i32 s4, s2, 0x3200
	s_waitcnt lgkmcnt(0)
	s_add_u32 s14, s8, 0xb700000
	v_and_b32_e32 v62, 15, v65
	s_addc_u32 s15, s9, 0
	s_waitcnt vmcnt(0)
	v_lshlrev_b64 v[4:5], 1, v[66:67]
	s_add_i32 s10, s4, 0
	v_cmp_gt_i32_e64 s[4:5], 2, v3
	v_lshlrev_b32_e32 v0, 3, v3
	v_cmp_lt_i32_e64 s[6:7], 1, v3
	v_lshl_add_u64 v[70:71], s[14:15], 0, v[4:5]
	v_mul_u32_u24_e32 v3, 0x210, v62
	v_and_b32_e32 v6, -16, v65
	v_lshl_add_u64 v[4:5], s[8:9], 0, v[4:5]
	s_mov_b64 s[8:9], 0x3ef80000
	s_load_dwordx4 s[16:19], s[0:1], 0x30
	s_load_dwordx2 s[20:21], s[0:1], 0x60
	v_add3_u32 v75, s10, v3, v6
	v_lshl_add_u64 v[72:73], v[4:5], 0, s[8:9]
	v_mov_b32_e32 v3, s10
	s_movk_i32 s8, 0x110
	v_readlane_b32 s11, v254, 38
	s_lshl_b32 s36, s2, 8
	v_mad_u32_u24 v3, v62, s8, v3
	s_lshl_b32 s8, s2, 9
	v_readlane_b32 s9, v254, 11
	s_lshl_b32 s35, s11, 6
	s_ashr_i32 s37, s36, 31
	v_and_b32_e32 v2, 8, v0
	s_lshl_b32 s96, s11, 10
	s_add_i32 s8, s9, s8
	v_ashrrev_i32_e32 v1, 31, v0
	v_lshlrev_b32_e32 v8, 1, v2
	v_lshlrev_b32_e32 v4, 3, v65
	s_cmp_gt_i32 s2, 0
	v_lshlrev_b32_e32 v74, 4, v62
	v_lshlrev_b32_e32 v64, 6, v62
	v_mov_b32_e32 v63, v9
	v_lshl_add_u64 v[68:69], s[14:15], 0, v[8:9]
	v_lshl_add_u32 v77, v65, 2, s10
	v_add_u32_e32 v79, s8, v4
	s_cselect_b64 s[22:23], -1, 0
	v_or_b32_e32 v76, 0x100, v74
	v_or_b32_e32 v78, 0x200, v74
	v_or_b32_e32 v80, 0x300, v74
	v_add_u32_e32 v81, s9, v4
	v_lshlrev_b32_e32 v82, 1, v2
	v_add_u32_e32 v110, v3, v6
	s_lshl_b64 s[24:25], s[96:97], 2
	v_lshlrev_b64 v[84:85], 2, v[0:1]
	s_branch .LBB0_414
.LBB0_413:
	s_add_i32 s34, s34, s3
	s_cmpk_gt_i32 s34, 0xff
	s_waitcnt vmcnt(0) lgkmcnt(0)
	s_barrier
	s_cbranch_scc1 .LBB0_505

; __global__ void __launch_bounds__(NWAVES * 64, 2) mk_fwd(Args args) {
;     ...
;                 for (int pass = 0; pass < 2; ++pass) {
;                     v4u uwn = *(const v4u*)(PROJ + (tok0 + i16) * DINP + U_OFF + g * 16 + 8 * (g4 & 1));
; #pragma unroll 1
;                     for (int st = 0; st < 16; ++st) {
;                         const size_t rowt = tok0 + st * 16 + i16;
;                         v4u uw = uwn; if (g4 >= 2) { uw.x = 0u; uw.y = 0u; uw.z = 0u; uw.w = 0u; }
;                         { const int stn = st < 15 ? st + 1 : 15; uwn = *(const v4u*)(PROJ + (tok0 + stn * 16 + i16) * DINP + U_OFF + g * 16 + 8 * (g4 & 1)); }
;                         const v2u uq = *(const v2u*)(PROJ + rowt * DINP + U_OFF + g * 16 + 4 * g4);
;     ...
;                             const f32x4 dsk = *(const f32x4*)(ka->in[13] + l * 1024 + g * 16 + 4 * g4);
.LBB0_465:
	s_waitcnt vmcnt(0)
	s_load_dwordx2 s[98:99], s[0:1], 0x68
	s_waitcnt lgkmcnt(0)
	s_add_u32 s98, s98, s24
	s_addc_u32 s99, s99, s25
	s_add_u32 s98, s98, s33
	s_addc_u32 s99, s99, 0
	v_lshl_add_u64 v[116:117], v[66:67], 2, s[98:99]
	global_load_dwordx4 v[116:119], v[116:117], off
	v_readlane_b32 s98, v254, 10
	v_mbcnt_lo_u32_b32 v138, -1, 0
	v_mbcnt_hi_u32_b32 v138, -1, v138
	s_nop 1
	s_lshl_b32 s98, s98, 12
	s_add_i32 s98, s98, 0x1a000
	v_mov_b32_e32 v139, s98
	v_lshrrev_b32_e32 v137, 5, v138
	v_and_b32_e32 v136, 15, v138
	v_lshl_add_u32 v137, v137, 4, v136
	v_lshlrev_b32_e32 v137, 4, v137
	v_bfe_u32 v136, v138, 4, 1
	v_lshl_add_u32 v137, v136, 3, v137
	v_add_u32_e32 v137, s98, v137
	v_and_b32_e32 v138, 31, v138
	v_lshl_add_u32 v138, v138, 4, v139
	v_mov_b32_e32 v52, v94
	v_mov_b32_e32 v53, v95
	s_add_i32 m0, s98, 0
	s_mov_b32 exec_hi, 0
	global_load_lds_dwordx4 v[52:53], off
	s_mov_b32 exec_hi, -1
	s_mov_b32 s99, 0
	s_mov_b32 s98, 0x78000
	v_lshl_add_u64 v[52:53], v[94:95], 0, s[98:99]
	v_readfirstlane_b32 s98, v139
	s_add_i32 m0, s98, 512
	s_mov_b32 exec_hi, 0
	global_load_lds_dwordx4 v[52:53], off
	s_mov_b32 exec_hi, -1
	s_mov_b32 s99, 0
	s_mov_b32 s98, 0xf0000
	v_lshl_add_u64 v[52:53], v[94:95], 0, s[98:99]
	v_readfirstlane_b32 s98, v139
	s_add_i32 m0, s98, 1024
	s_mov_b32 exec_hi, 0
	global_load_lds_dwordx4 v[52:53], off
	s_mov_b32 exec_hi, -1
	s_mov_b32 s99, 0
	s_mov_b32 s98, 0x168000
	v_lshl_add_u64 v[52:53], v[94:95], 0, s[98:99]
	v_readfirstlane_b32 s98, v139
	s_add_i32 m0, s98, 1536
	s_mov_b32 exec_hi, 0
	global_load_lds_dwordx4 v[52:53], off
	s_mov_b32 exec_hi, -1
	s_xor_b64 s[26:27], s[10:11], -1
	s_mov_b64 s[28:29], 0
	s_branch .LBB0_467

; __device__ __forceinline__ unsigned cvt_pk_bf16(float lo, float hi) { unsigned r; asm volatile("v_cvt_pk_bf16_f32 %0, %1, %2" : "=v"(r) : "v"(lo), "v"(hi)); return r; }
; #define LAS __attribute__((address_space(3)))
; __global__ void __launch_bounds__(NWAVES * 64, 2) mk_fwd(Args args) {
;     ...
;                     v4u uwn = *(const v4u*)(PROJ + (tok0 + i16) * DINP + U_OFF + g * 16 + 8 * (g4 & 1));
; #pragma unroll 1
;                     for (int st = 0; st < 16; ++st) {
;                         const size_t rowt = tok0 + st * 16 + i16;
;                         v4u uw = uwn; if (g4 >= 2) { uw.x = 0u; uw.y = 0u; uw.z = 0u; uw.w = 0u; }
;                         { const int stn = st < 15 ? st + 1 : 15; uwn = *(const v4u*)(PROJ + (tok0 + stn * 16 + i16) * DINP + U_OFF + g * 16 + 8 * (g4 & 1)); }
;                         const v2u uq = *(const v2u*)(PROJ + rowt * DINP + U_OFF + g * 16 + 4 * g4);
;                         const pg8::bf16x8 Uop = __builtin_bit_cast(pg8::bf16x8, uw);
; #pragma unroll
;                         for (int mt = 0; mt < 8; ++mt) { f32x4 d = {0.f, 0.f, 0.f, 0.f}; d = __builtin_amdgcn_mfma_f32_16x16x32_bf16(Abb[mt], Uop, d, 0, 0, 0);
;                             *(LAS f32x4*)(BUs + i16 * 132 + 16 * mt + 4 * g4) = d; }
;                         asm volatile("s_waitcnt lgkmcnt(0)" ::: "memory");
; #pragma unroll
;                         for (int tt = 0; tt < 16; ++tt) {
;                             const float bur = BUs[tt * 132 + lane], bui = BUs[tt * 132 + 64 + lane];
;                             const float nr = ab_re * s_re - ab_im * s_im + bur, ni = ab_re * s_im + ab_im * s_re + bui; s_re = nr; s_im = ni;
;                             if (pass == 1) Ss[tt * 68 + lane] = cvt_pk_bf16(s_re, s_im);
;                         }
.LBB0_467:
	s_mov_b64 s[8:9], s[28:29]
	s_add_u32 s28, s8, 16
	v_lshl_add_u64 v[54:55], v[62:63], 0, s[8:9]
	s_addc_u32 s29, s9, 0
	v_or_b32_e32 v106, s30, v54
	v_or_b32_e32 v107, s31, v55
	s_lshl_b32 s99, s8, 5
	s_and_b32 s99, s99, 0xe00
	v_add_u32_e32 v136, s99, v138
	v_add_u32_e32 v135, s99, v137
	s_waitcnt vmcnt(3)
	ds_read_b128 v[54:57], v136
	ds_read_b64 v[108:109], v135
	s_add_i32 s96, s8, 64
	s_min_i32 s96, s96, 0xf0
	s_mul_i32 s98, s96, 0x7800
	s_mov_b32 s99, 0
	v_lshl_add_u64 v[52:53], v[94:95], 0, s[98:99]
	v_readfirstlane_b32 s98, v139
	s_add_i32 s99, s8, 64
	s_lshl_b32 s99, s99, 5
	s_and_b32 s99, s99, 0xe00
	s_add_i32 m0, s98, s99
	s_mov_b32 exec_hi, 0
	global_load_lds_dwordx4 v[52:53], off
	s_mov_b32 exec_hi, -1
	s_waitcnt lgkmcnt(0)
	v_cndmask_b32_e64 v54, v54, 0, s[6:7]
	v_cndmask_b32_e64 v55, v55, 0, s[6:7]
	v_cndmask_b32_e64 v56, v56, 0, s[6:7]
	v_cndmask_b32_e64 v57, v57, 0, s[6:7]
	s_nop 1
	v_mfma_f32_16x16x32_bf16 v[180:183], v[0:3], v[54:57], 0
	v_mfma_f32_16x16x32_bf16 v[184:187], v[10:13], v[54:57], 0
	v_mfma_f32_16x16x32_bf16 v[188:191], v[18:21], v[54:57], 0
	v_mfma_f32_16x16x32_bf16 v[192:195], v[26:29], v[54:57], 0
	v_mfma_f32_16x16x32_bf16 v[196:199], v[4:7], v[54:57], 0
	v_mfma_f32_16x16x32_bf16 v[200:203], v[14:17], v[54:57], 0
	v_mfma_f32_16x16x32_bf16 v[204:207], v[22:25], v[54:57], 0
	v_mfma_f32_16x16x32_bf16 v[208:211], v[30:33], v[54:57], 0
	s_nop 0
	ds_write_b128 v75, v[180:183]
	ds_write_b128 v75, v[184:187] offset:64
	ds_write_b128 v75, v[188:191] offset:128
	ds_write_b128 v75, v[192:195] offset:192
	ds_write_b128 v75, v[196:199] offset:256
	ds_write_b128 v75, v[200:203] offset:320
	ds_write_b128 v75, v[204:207] offset:384
	ds_write_b128 v75, v[208:211] offset:448
	s_waitcnt lgkmcnt(0)
	ds_read_b32 v148, v77
	ds_read_b32 v149, v77 offset:256
	ds_read_b32 v150, v77 offset:528
	ds_read_b32 v151, v77 offset:784
	ds_read_b32 v152, v77 offset:1056
	ds_read_b32 v153, v77 offset:1312
	ds_read_b32 v154, v77 offset:1584
	ds_read_b32 v155, v77 offset:1840
	ds_read_b32 v156, v77 offset:2112
	ds_read_b32 v157, v77 offset:2368
	ds_read_b32 v158, v77 offset:2640
	ds_read_b32 v159, v77 offset:2896
	ds_read_b32 v160, v77 offset:3168
	ds_read_b32 v161, v77 offset:3424
	ds_read_b32 v162, v77 offset:3696
	ds_read_b32 v163, v77 offset:3952
	ds_read_b32 v164, v77 offset:4224
	ds_read_b32 v165, v77 offset:4480
	ds_read_b32 v166, v77 offset:4752
	ds_read_b32 v167, v77 offset:5008
	ds_read_b32 v168, v77 offset:5280
	ds_read_b32 v169, v77 offset:5536
	ds_read_b32 v170, v77 offset:5808
	ds_read_b32 v171, v77 offset:6064
	ds_read_b32 v172, v77 offset:6336
	ds_read_b32 v173, v77 offset:6592
	ds_read_b32 v174, v77 offset:6864
	ds_read_b32 v175, v77 offset:7120
	ds_read_b32 v176, v77 offset:7392
	ds_read_b32 v177, v77 offset:7648
	ds_read_b32 v178, v77 offset:7920
	ds_read_b32 v179, v77 offset:8176
	s_and_b64 vcc, exec, s[12:13]
	s_waitcnt lgkmcnt(0)
	s_cbranch_vccnz .Lmy_s5_p1
	v_fma_f32 v148, -v90, v87, v148
	v_fma_f32 v149, v90, v86, v149
	v_fma_f32 v86, v88, v86, v148
	v_fma_f32 v87, v88, v87, v149
	v_fma_f32 v150, -v90, v87, v150
	v_fma_f32 v151, v90, v86, v151
	v_fma_f32 v86, v88, v86, v150
	v_fma_f32 v87, v88, v87, v151
	v_fma_f32 v152, -v90, v87, v152
	v_fma_f32 v153, v90, v86, v153
	v_fma_f32 v86, v88, v86, v152
	v_fma_f32 v87, v88, v87, v153
	v_fma_f32 v154, -v90, v87, v154
	v_fma_f32 v155, v90, v86, v155
	v_fma_f32 v86, v88, v86, v154
	v_fma_f32 v87, v88, v87, v155
	v_fma_f32 v156, -v90, v87, v156
	v_fma_f32 v157, v90, v86, v157
	v_fma_f32 v86, v88, v86, v156
	v_fma_f32 v87, v88, v87, v157
	v_fma_f32 v158, -v90, v87, v158
	v_fma_f32 v159, v90, v86, v159
	v_fma_f32 v86, v88, v86, v158
	v_fma_f32 v87, v88, v87, v159
	v_fma_f32 v160, -v90, v87, v160
	v_fma_f32 v161, v90, v86, v161
	v_fma_f32 v86, v88, v86, v160
	v_fma_f32 v87, v88, v87, v161
	v_fma_f32 v162, -v90, v87, v162
	v_fma_f32 v163, v90, v86, v163
	v_fma_f32 v86, v88, v86, v162
	v_fma_f32 v87, v88, v87, v163
	v_fma_f32 v164, -v90, v87, v164
	v_fma_f32 v165, v90, v86, v165
	v_fma_f32 v86, v88, v86, v164
	v_fma_f32 v87, v88, v87, v165
	v_fma_f32 v166, -v90, v87, v166
	v_fma_f32 v167, v90, v86, v167
	v_fma_f32 v86, v88, v86, v166
	v_fma_f32 v87, v88, v87, v167
	v_fma_f32 v168, -v90, v87, v168
	v_fma_f32 v169, v90, v86, v169
	v_fma_f32 v86, v88, v86, v168
	v_fma_f32 v87, v88, v87, v169
	v_fma_f32 v170, -v90, v87, v170
	v_fma_f32 v171, v90, v86, v171
	v_fma_f32 v86, v88, v86, v170
	v_fma_f32 v87, v88, v87, v171
	v_fma_f32 v172, -v90, v87, v172
	v_fma_f32 v173, v90, v86, v173
	v_fma_f32 v86, v88, v86, v172
	v_fma_f32 v87, v88, v87, v173
	v_fma_f32 v174, -v90, v87, v174
	v_fma_f32 v175, v90, v86, v175
	v_fma_f32 v86, v88, v86, v174
	v_fma_f32 v87, v88, v87, v175
	v_fma_f32 v176, -v90, v87, v176
	v_fma_f32 v177, v90, v86, v177
	v_fma_f32 v86, v88, v86, v176
	v_fma_f32 v87, v88, v87, v177
	v_fma_f32 v178, -v90, v87, v178
	v_fma_f32 v179, v90, v86, v179
	v_fma_f32 v86, v88, v86, v178
	v_fma_f32 v87, v88, v87, v179
	s_branch .LBB0_466
; __device__ __forceinline__ unsigned cvt_pk_bf16(float lo, float hi) { unsigned r; asm volatile("v_cvt_pk_bf16_f32 %0, %1, %2" : "=v"(r) : "v"(lo), "v"(hi)); return r; }
; #define LAS __attribute__((address_space(3)))
; __global__ void __launch_bounds__(NWAVES * 64, 2) mk_fwd(Args args) {
;     ...
;                         for (int tt = 0; tt < 16; ++tt) {
;                             const float bur = BUs[tt * 132 + lane], bui = BUs[tt * 132 + 64 + lane];
;                             const float nr = ab_re * s_re - ab_im * s_im + bur, ni = ab_re * s_im + ab_im * s_re + bui; s_re = nr; s_im = ni;
;                             if (pass == 1) Ss[tt * 68 + lane] = cvt_pk_bf16(s_re, s_im);
;                         }
;                         asm volatile("s_waitcnt lgkmcnt(0)" ::: "memory");
;                         if (pass == 1) {
;                             f32x4 y = {0.f, 0.f, 0.f, 0.f};
; #pragma unroll
;                             for (int kb = 0; kb < 4; ++kb) { const pg8::bf16x8 Sop = *(const LAS pg8::bf16x8*)((const LAS unsigned char*)Ss + i16 * 272 + 64 * kb + 16 * g4);
;                                 y = __builtin_amdgcn_mfma_f32_16x16x32_bf16(Cop[kb], Sop, y, 0, 0, 0); }
;                             const f32x4 dsk = *(const f32x4*)(ka->in[13] + l * 1024 + g * 16 + 4 * g4);
;                             const float uu[4] = {bflo(uq.x), bfhi(uq.x), bflo(uq.y), bfhi(uq.y)}; float zz[4];
.Lmy_s5_p1:
	v_fma_f32 v148, -v90, v87, v148
	v_fma_f32 v149, v90, v86, v149
	v_fma_f32 v86, v88, v86, v148
	v_fma_f32 v87, v88, v87, v149
	v_cvt_pk_bf16_f32 v148, v86, v87
	ds_write_b32 v77, v148 offset:8448
	v_fma_f32 v150, -v90, v87, v150
	v_fma_f32 v151, v90, v86, v151
	v_fma_f32 v86, v88, v86, v150
	v_fma_f32 v87, v88, v87, v151
	v_cvt_pk_bf16_f32 v150, v86, v87
	ds_write_b32 v77, v150 offset:8720
	v_fma_f32 v152, -v90, v87, v152
	v_fma_f32 v153, v90, v86, v153
	v_fma_f32 v86, v88, v86, v152
	v_fma_f32 v87, v88, v87, v153
	v_cvt_pk_bf16_f32 v152, v86, v87
	ds_write_b32 v77, v152 offset:8992
	v_fma_f32 v154, -v90, v87, v154
	v_fma_f32 v155, v90, v86, v155
	v_fma_f32 v86, v88, v86, v154
	v_fma_f32 v87, v88, v87, v155
	v_cvt_pk_bf16_f32 v154, v86, v87
	ds_write_b32 v77, v154 offset:9264
	v_fma_f32 v156, -v90, v87, v156
	v_fma_f32 v157, v90, v86, v157
	v_fma_f32 v86, v88, v86, v156
	v_fma_f32 v87, v88, v87, v157
	v_cvt_pk_bf16_f32 v156, v86, v87
	ds_write_b32 v77, v156 offset:9536
	v_fma_f32 v158, -v90, v87, v158
	v_fma_f32 v159, v90, v86, v159
	v_fma_f32 v86, v88, v86, v158
	v_fma_f32 v87, v88, v87, v159
	v_cvt_pk_bf16_f32 v158, v86, v87
	ds_write_b32 v77, v158 offset:9808
	v_fma_f32 v160, -v90, v87, v160
	v_fma_f32 v161, v90, v86, v161
	v_fma_f32 v86, v88, v86, v160
	v_fma_f32 v87, v88, v87, v161
	v_cvt_pk_bf16_f32 v160, v86, v87
	ds_write_b32 v77, v160 offset:10080
	v_fma_f32 v162, -v90, v87, v162
	v_fma_f32 v163, v90, v86, v163
	v_fma_f32 v86, v88, v86, v162
	v_fma_f32 v87, v88, v87, v163
	v_cvt_pk_bf16_f32 v162, v86, v87
	ds_write_b32 v77, v162 offset:10352
	v_fma_f32 v164, -v90, v87, v164
	v_fma_f32 v165, v90, v86, v165
	v_fma_f32 v86, v88, v86, v164
	v_fma_f32 v87, v88, v87, v165
	v_cvt_pk_bf16_f32 v164, v86, v87
	ds_write_b32 v77, v164 offset:10624
	v_fma_f32 v166, -v90, v87, v166
	v_fma_f32 v167, v90, v86, v167
	v_fma_f32 v86, v88, v86, v166
	v_fma_f32 v87, v88, v87, v167
	v_cvt_pk_bf16_f32 v166, v86, v87
	ds_write_b32 v77, v166 offset:10896
	v_fma_f32 v168, -v90, v87, v168
	v_fma_f32 v169, v90, v86, v169
	v_fma_f32 v86, v88, v86, v168
	v_fma_f32 v87, v88, v87, v169
	v_cvt_pk_bf16_f32 v168, v86, v87
	ds_write_b32 v77, v168 offset:11168
	v_fma_f32 v170, -v90, v87, v170
	v_fma_f32 v171, v90, v86, v171
	v_fma_f32 v86, v88, v86, v170
	v_fma_f32 v87, v88, v87, v171
	v_cvt_pk_bf16_f32 v170, v86, v87
	ds_write_b32 v77, v170 offset:11440
	v_fma_f32 v172, -v90, v87, v172
	v_fma_f32 v173, v90, v86, v173
	v_fma_f32 v86, v88, v86, v172
	v_fma_f32 v87, v88, v87, v173
	v_cvt_pk_bf16_f32 v172, v86, v87
	ds_write_b32 v77, v172 offset:11712
	v_fma_f32 v174, -v90, v87, v174
	v_fma_f32 v175, v90, v86, v175
	v_fma_f32 v86, v88, v86, v174
	v_fma_f32 v87, v88, v87, v175
	v_cvt_pk_bf16_f32 v174, v86, v87
	ds_write_b32 v77, v174 offset:11984
	v_fma_f32 v176, -v90, v87, v176
	v_fma_f32 v177, v90, v86, v177
	v_fma_f32 v86, v88, v86, v176
	v_fma_f32 v87, v88, v87, v177
	v_cvt_pk_bf16_f32 v176, v86, v87
	ds_write_b32 v77, v176 offset:12256
	v_fma_f32 v178, -v90, v87, v178
	v_fma_f32 v179, v90, v86, v179
	v_fma_f32 v86, v88, v86, v178
	v_fma_f32 v87, v88, v87, v179
	v_cvt_pk_bf16_f32 v178, v86, v87
	ds_write_b32 v77, v178 offset:12528
	s_waitcnt lgkmcnt(0)
	ds_read_b128 v[54:57], v110 offset:8448
	ds_read_b128 v[58:61], v110 offset:8512
	s_nop 0
	v_lshlrev_b32_e32 v8, 16, v108
	v_and_b32_e32 v83, 0xffff0000, v108
	s_waitcnt lgkmcnt(0)
	v_mfma_f32_16x16x32_bf16 v[54:57], v[34:37], v[54:57], 0
	v_lshlrev_b32_e32 v108, 16, v109
	v_mfma_f32_16x16x32_bf16 v[54:57], v[38:41], v[58:61], v[54:57]
	ds_read_b128 v[58:61], v110 offset:8576
	v_and_b32_e32 v109, 0xffff0000, v109
	s_waitcnt lgkmcnt(0)
; __device__ __forceinline__ unsigned cvt_pk_bf16(float lo, float hi) { unsigned r; asm volatile("v_cvt_pk_bf16_f32 %0, %1, %2" : "=v"(r) : "v"(lo), "v"(hi)); return r; }
; #define LAS __attribute__((address_space(3)))
; __global__ void __launch_bounds__(NWAVES * 64, 2) mk_fwd(Args args) {
;     ...
;                             for (int kb = 0; kb < 4; ++kb) { const pg8::bf16x8 Sop = *(const LAS pg8::bf16x8*)((const LAS unsigned char*)Ss + i16 * 272 + 64 * kb + 16 * g4);
;                                 y = __builtin_amdgcn_mfma_f32_16x16x32_bf16(Cop[kb], Sop, y, 0, 0, 0); }
;                             const f32x4 dsk = *(const f32x4*)(ka->in[13] + l * 1024 + g * 16 + 4 * g4);
;                             const float uu[4] = {bflo(uq.x), bfhi(uq.x), bflo(uq.y), bfhi(uq.y)}; float zz[4];
; #pragma unroll
;                             for (int i = 0; i < 4; ++i) { const float yy = y[i] + dsk[i] * uu[i]; const float a = 0.7978845608028654f * (yy + 0.044715f * yy * yy * yy);
;                                 const float th = 1.0f - 2.0f / (1.0f + __expf(2.0f * a)); zz[i] = 0.5f * yy * (1.0f + th); }
;                             v2u zo; zo.x = cvt_pk_bf16(zz[0], zz[1]); zo.y = cvt_pk_bf16(zz[2], zz[3]);
;                             *(v2u*)(Z + rowt * 1024 + g * 16 + 4 * g4) = zo;
	v_mfma_f32_16x16x32_bf16 v[54:57], v[42:45], v[58:61], v[54:57]
	ds_read_b128 v[58:61], v110 offset:8640
	s_waitcnt lgkmcnt(0)
	v_mfma_f32_16x16x32_bf16 v[54:57], v[46:49], v[58:61], v[54:57]
	s_nop 7
	v_fma_f32 v8, v116, v8, v54
	v_mul_f32_e32 v54, 0x3d372713, v8
	v_mul_f32_e32 v54, v8, v54
	v_fma_f32 v54, v8, v54, v8
	v_mul_f32_e32 v54, 0x3f4c422a, v54
	v_add_f32_e32 v54, v54, v54
	v_mul_f32_e32 v54, 0x3fb8aa3b, v54
	v_exp_f32_e32 v54, v54
	v_mul_f32_e32 v8, 0.5, v8
	v_fmac_f32_e32 v57, v119, v109
	v_add_f32_e32 v54, 1.0, v54
	v_div_scale_f32 v58, s[8:9], v54, v54, 2.0
	v_rcp_f32_e32 v111, v58
	s_nop 0
	v_fma_f32 v112, -v58, v111, 1.0
	v_fmac_f32_e32 v111, v112, v111
	v_div_scale_f32 v112, vcc, 2.0, v54, 2.0
	v_mul_f32_e32 v113, v112, v111
	v_fma_f32 v114, -v58, v113, v112
	v_fmac_f32_e32 v113, v114, v111
	v_fma_f32 v58, -v58, v113, v112
	v_div_fmas_f32 v58, v58, v111, v113
	v_div_fixup_f32 v54, v58, v54, 2.0
	v_sub_f32_e32 v54, 1.0, v54
	v_add_f32_e32 v54, 1.0, v54
	v_mul_f32_e32 v8, v8, v54
	v_fma_f32 v54, v117, v83, v55
	v_mul_f32_e32 v55, 0x3d372713, v54
	v_mul_f32_e32 v55, v54, v55
	v_fma_f32 v55, v54, v55, v54
	v_mul_f32_e32 v55, 0x3f4c422a, v55
	v_add_f32_e32 v55, v55, v55
	v_mul_f32_e32 v55, 0x3fb8aa3b, v55
	v_exp_f32_e32 v55, v55
	v_mul_f32_e32 v54, 0.5, v54
	v_add_f32_e32 v55, 1.0, v55
	v_div_scale_f32 v58, s[8:9], v55, v55, 2.0
	v_rcp_f32_e32 v59, v58
	s_nop 0
	v_fma_f32 v83, -v58, v59, 1.0
	v_fmac_f32_e32 v59, v83, v59
	v_div_scale_f32 v83, vcc, 2.0, v55, 2.0
	v_mul_f32_e32 v111, v83, v59
	v_fma_f32 v112, -v58, v111, v83
	v_fmac_f32_e32 v111, v112, v59
	v_fma_f32 v58, -v58, v111, v83
	v_div_fmas_f32 v58, v58, v59, v111
	v_div_fixup_f32 v55, v58, v55, 2.0
	v_sub_f32_e32 v55, 1.0, v55
	v_add_f32_e32 v55, 1.0, v55
	v_mul_f32_e32 v54, v54, v55
	v_fma_f32 v55, v118, v108, v56
	v_mul_f32_e32 v56, 0x3d372713, v55
	v_mul_f32_e32 v56, v55, v56
	v_fma_f32 v56, v55, v56, v55
	v_mul_f32_e32 v56, 0x3f4c422a, v56
	v_add_f32_e32 v56, v56, v56
	v_mul_f32_e32 v56, 0x3fb8aa3b, v56
	v_exp_f32_e32 v56, v56
	v_mul_f32_e32 v55, 0.5, v55
	v_cvt_pk_bf16_f32 v54, v8, v54
	v_add_f32_e32 v56, 1.0, v56
	v_div_scale_f32 v58, s[8:9], v56, v56, 2.0
	v_rcp_f32_e32 v59, v58
	s_nop 0
	v_fma_f32 v60, -v58, v59, 1.0
	v_fmac_f32_e32 v59, v60, v59
	v_div_scale_f32 v60, vcc, 2.0, v56, 2.0
	v_mul_f32_e32 v83, v60, v59
	v_fma_f32 v108, -v58, v83, v60
	v_fmac_f32_e32 v83, v108, v59
	v_fma_f32 v58, -v58, v83, v60
	v_div_fmas_f32 v58, v58, v59, v83
	v_div_fixup_f32 v56, v58, v56, 2.0
	v_sub_f32_e32 v56, 1.0, v56
	v_add_f32_e32 v56, 1.0, v56
	v_mul_f32_e32 v55, v55, v56
	v_mul_f32_e32 v56, 0x3d372713, v57
	v_mul_f32_e32 v56, v57, v56
	v_fma_f32 v56, v57, v56, v57
	v_mul_f32_e32 v56, 0x3f4c422a, v56
	v_add_f32_e32 v56, v56, v56
	v_mul_f32_e32 v56, 0x3fb8aa3b, v56
	v_exp_f32_e32 v56, v56
	v_mul_f32_e32 v57, 0.5, v57
	v_add_f32_e32 v56, 1.0, v56
	v_div_scale_f32 v58, s[8:9], v56, v56, 2.0
	v_rcp_f32_e32 v59, v58
	s_nop 0
	v_fma_f32 v60, -v58, v59, 1.0
	v_fmac_f32_e32 v59, v60, v59
	v_div_scale_f32 v60, vcc, 2.0, v56, 2.0
	v_mul_f32_e32 v61, v60, v59
	v_fma_f32 v83, -v58, v61, v60
	v_fmac_f32_e32 v61, v83, v59
	v_fma_f32 v58, -v58, v61, v60
	v_div_fmas_f32 v58, v58, v59, v61
	v_div_fixup_f32 v56, v58, v56, 2.0
	v_sub_f32_e32 v56, 1.0, v56
	v_add_f32_e32 v56, 1.0, v56
	v_mul_f32_e32 v56, v57, v56
	v_cvt_pk_bf16_f32 v55, v55, v56
	v_lshlrev_b64 v[56:57], 11, v[106:107]
	v_lshl_add_u64 v[56:57], v[100:101], 0, v[56:57]
	global_store_dwordx2 v[56:57], v[54:55], off
	s_waitcnt lgkmcnt(0)
	s_branch .LBB0_466
